# gather v-section ring waits relaxed by 3 (7-8 rows in flight in v loops, 7 in u loops)
# speedup vs baseline: 1.0658x; 1.0048x over previous
.Lnb_1423:
.LBB0_1423:
	s_add_i32 s57, s56, 0xffffff61
	s_waitcnt vmcnt(8)
	v_perm_b32 v112, v14, v6, s67
	v_perm_b32 v6, v14, v6, s68
	s_waitcnt vmcnt(6)
	v_perm_b32 v14, v46, v30, s67
	v_readlane_b32 s57, v111, s57
	v_perm_b32 v30, v46, v30, s68
	v_perm_b32 v46, v14, v112, s69
	v_perm_b32 v14, v14, v112, s33
	v_perm_b32 v112, v30, v6, s69
	v_perm_b32 v6, v30, v6, s33
	v_dot4c_i32_i8_e32 v74, s57, v14
	v_and_b32_e32 v14, 0xf0f0f0f0, v14
	v_dot4c_i32_i8_e32 v70, s57, v14
	v_and_b32_e32 v14, 0xf0f0f0f0, v112
	v_dot4c_i32_i8_e32 v76, s57, v6
	v_and_b32_e32 v6, 0xf0f0f0f0, v6
	v_and_b32_e32 v30, 0xf0f0f0f0, v46
	v_dot4c_i32_i8_e32 v72, s57, v14
	v_dot4c_i32_i8_e32 v73, s57, v6
	v_perm_b32 v6, v15, v7, s67
	v_perm_b32 v14, v47, v31, s67
	v_dot4c_i32_i8_e32 v69, s57, v30
	v_perm_b32 v7, v15, v7, s68
	v_perm_b32 v15, v47, v31, s68
	v_perm_b32 v30, v14, v6, s69
	v_perm_b32 v6, v14, v6, s33
	v_perm_b32 v14, v15, v7, s69
	v_dot4c_i32_i8_e32 v85, s57, v6
	v_and_b32_e32 v6, 0xf0f0f0f0, v6
	v_perm_b32 v7, v15, v7, s33
	v_dot4c_i32_i8_e32 v81, s57, v6
	v_and_b32_e32 v6, 0xf0f0f0f0, v14
	v_dot4c_i32_i8_e32 v82, s57, v6
	v_and_b32_e32 v6, 0xf0f0f0f0, v7
	v_and_b32_e32 v15, 0xf0f0f0f0, v30
	v_dot4c_i32_i8_e32 v94, s57, v7
	v_dot4c_i32_i8_e32 v84, s57, v6
	v_perm_b32 v6, v16, v8, s67
	v_perm_b32 v7, v16, v8, s68
	v_perm_b32 v8, v48, v32, s67
	v_dot4c_i32_i8_e32 v77, s57, v15
	v_dot4c_i32_i8_e32 v86, s57, v14
	v_perm_b32 v14, v48, v32, s68
	v_perm_b32 v15, v8, v6, s69
	v_perm_b32 v6, v8, v6, s33
	v_perm_b32 v8, v14, v7, s69
	v_dot4c_i32_i8_e32 v96, s57, v6
	v_and_b32_e32 v6, 0xf0f0f0f0, v6
	v_perm_b32 v7, v14, v7, s33
	v_dot4c_i32_i8_e32 v88, s57, v6
	v_and_b32_e32 v6, 0xf0f0f0f0, v8
	v_dot4c_i32_i8_e32 v89, s57, v6
	v_and_b32_e32 v6, 0xf0f0f0f0, v7
	v_and_b32_e32 v14, 0xf0f0f0f0, v15
	v_dot4c_i32_i8_e32 v97, s57, v8
	v_dot4c_i32_i8_e32 v90, s57, v6
	v_perm_b32 v6, v17, v9, s67
	v_perm_b32 v8, v49, v33, s67
	v_dot4c_i32_i8_e32 v87, s57, v14
	v_dot4c_i32_i8_e32 v98, s57, v7
	v_perm_b32 v7, v17, v9, s68
	v_perm_b32 v9, v49, v33, s68
	v_perm_b32 v14, v8, v6, s69
	v_perm_b32 v6, v8, v6, s33
	v_perm_b32 v8, v9, v7, s69
	v_dot4c_i32_i8_e32 v100, s57, v6
	v_and_b32_e32 v6, 0xf0f0f0f0, v6
	v_perm_b32 v7, v9, v7, s33
	v_dot4c_i32_i8_e32 v92, s57, v6
	v_and_b32_e32 v6, 0xf0f0f0f0, v8
	v_and_b32_e32 v9, 0xf0f0f0f0, v14
	v_dot4c_i32_i8_e32 v93, s57, v6
	v_and_b32_e32 v6, 0xf0f0f0f0, v7
	v_dot4c_i32_i8_e32 v66, s57, v46
	v_dot4c_i32_i8_e32 v75, s57, v112
	v_dot4c_i32_i8_e32 v80, s57, v30
	v_dot4c_i32_i8_e32 v95, s57, v15
	v_dot4c_i32_i8_e32 v99, s57, v14
	v_dot4c_i32_i8_e32 v91, s57, v9
	v_dot4c_i32_i8_e32 v101, s57, v8
	v_dot4c_i32_i8_e32 v102, s57, v7
	v_dot4c_i32_i8_e32 v83, s57, v6
	s_add_i32 s57, s56, -15
	s_bitcmp0_b32 s57, 6
	s_cselect_b64 vcc, -1, 0
	v_cndmask_b32_e32 v6, v79, v78, vcc
	s_nop 0
	v_readlane_b32 s57, v6, s57
	s_lshl_b32 s57, s57, 10
	s_add_i32 s57, s57, 0x1000000
	s_nop 2
	buffer_load_dwordx4 v[6:9], v0, s[92:95], s57 offen
	s_add_i32 s57, s56, -14
	s_bitcmp0_b32 s57, 6
	s_cselect_b64 vcc, -1, 0
	v_cndmask_b32_e32 v14, v79, v78, vcc
	s_nop 0
	v_readlane_b32 s57, v14, s57
	s_lshl_b32 s57, s57, 10
	s_add_i32 s57, s57, 0x1000000
	s_nop 2
	buffer_load_dwordx4 v[14:17], v0, s[92:95], s57 offen
	s_add_i32 s57, s56, -13
	s_bitcmp0_b32 s57, 6
	s_cselect_b64 vcc, -1, 0
	v_cndmask_b32_e32 v30, v79, v78, vcc
	s_nop 0
	v_readlane_b32 s57, v30, s57
	s_lshl_b32 s57, s57, 10
	s_add_i32 s57, s57, 0x1000000
	s_nop 2
	buffer_load_dwordx4 v[30:33], v0, s[92:95], s57 offen
	s_add_i32 s57, s56, -12
	s_bitcmp0_b32 s57, 6
	s_cselect_b64 vcc, -1, 0
	v_cndmask_b32_e32 v46, v79, v78, vcc
	s_nop 0
	v_readlane_b32 s57, v46, s57
	s_lshl_b32 s57, s57, 10
	s_add_i32 s57, s57, 0x1000000
	s_nop 2
	buffer_load_dwordx4 v[46:49], v0, s[92:95], s57 offen
	s_add_i32 s57, s56, 0xffffff65
	s_waitcnt vmcnt(8)
	v_perm_b32 v112, v22, v2, s67
	v_perm_b32 v2, v22, v2, s68
	s_waitcnt vmcnt(6)
	v_perm_b32 v22, v54, v38, s67
	v_readlane_b32 s57, v111, s57
	v_perm_b32 v38, v54, v38, s68
	v_perm_b32 v54, v22, v112, s69
	v_perm_b32 v22, v22, v112, s33
	v_perm_b32 v112, v38, v2, s69
	v_perm_b32 v2, v38, v2, s33
	v_dot4c_i32_i8_e32 v74, s57, v22
	v_and_b32_e32 v22, 0xf0f0f0f0, v22
	v_dot4c_i32_i8_e32 v70, s57, v22
	v_and_b32_e32 v22, 0xf0f0f0f0, v112
	v_dot4c_i32_i8_e32 v76, s57, v2
	v_and_b32_e32 v2, 0xf0f0f0f0, v2
	v_and_b32_e32 v38, 0xf0f0f0f0, v54
	v_dot4c_i32_i8_e32 v72, s57, v22
	v_dot4c_i32_i8_e32 v73, s57, v2
	v_perm_b32 v2, v23, v3, s67
	v_perm_b32 v22, v55, v39, s67
	v_dot4c_i32_i8_e32 v69, s57, v38
	v_perm_b32 v3, v23, v3, s68
	v_perm_b32 v23, v55, v39, s68
	v_perm_b32 v38, v22, v2, s69
	v_perm_b32 v2, v22, v2, s33
	v_perm_b32 v22, v23, v3, s69
	v_dot4c_i32_i8_e32 v85, s57, v2
	v_and_b32_e32 v2, 0xf0f0f0f0, v2
	v_perm_b32 v3, v23, v3, s33
	v_dot4c_i32_i8_e32 v81, s57, v2
	v_and_b32_e32 v2, 0xf0f0f0f0, v22
	v_dot4c_i32_i8_e32 v82, s57, v2
	v_and_b32_e32 v2, 0xf0f0f0f0, v3
	v_and_b32_e32 v23, 0xf0f0f0f0, v38
	v_dot4c_i32_i8_e32 v94, s57, v3
	v_dot4c_i32_i8_e32 v84, s57, v2
	v_perm_b32 v2, v24, v4, s67
	v_perm_b32 v3, v24, v4, s68
	v_perm_b32 v4, v56, v40, s67
	v_dot4c_i32_i8_e32 v77, s57, v23
	v_dot4c_i32_i8_e32 v86, s57, v22
	v_perm_b32 v22, v56, v40, s68
	v_perm_b32 v23, v4, v2, s69
	v_perm_b32 v2, v4, v2, s33
	v_perm_b32 v4, v22, v3, s69
	v_dot4c_i32_i8_e32 v96, s57, v2
	v_and_b32_e32 v2, 0xf0f0f0f0, v2
	v_perm_b32 v3, v22, v3, s33
	v_dot4c_i32_i8_e32 v88, s57, v2
	v_and_b32_e32 v2, 0xf0f0f0f0, v4
	v_dot4c_i32_i8_e32 v89, s57, v2
	v_and_b32_e32 v2, 0xf0f0f0f0, v3
	v_and_b32_e32 v22, 0xf0f0f0f0, v23
	v_dot4c_i32_i8_e32 v97, s57, v4
	v_dot4c_i32_i8_e32 v90, s57, v2
	v_perm_b32 v2, v25, v5, s67
	v_perm_b32 v4, v57, v41, s67
	v_dot4c_i32_i8_e32 v87, s57, v22
	v_dot4c_i32_i8_e32 v98, s57, v3
	v_perm_b32 v3, v25, v5, s68
	v_perm_b32 v5, v57, v41, s68
	v_perm_b32 v22, v4, v2, s69
	v_perm_b32 v2, v4, v2, s33
	v_perm_b32 v4, v5, v3, s69
	v_dot4c_i32_i8_e32 v100, s57, v2
	v_and_b32_e32 v2, 0xf0f0f0f0, v2
	v_perm_b32 v3, v5, v3, s33
	v_dot4c_i32_i8_e32 v92, s57, v2
	v_and_b32_e32 v2, 0xf0f0f0f0, v4
	v_and_b32_e32 v5, 0xf0f0f0f0, v22
	v_dot4c_i32_i8_e32 v93, s57, v2
	v_and_b32_e32 v2, 0xf0f0f0f0, v3
	v_dot4c_i32_i8_e32 v66, s57, v54
	v_dot4c_i32_i8_e32 v75, s57, v112
	v_dot4c_i32_i8_e32 v80, s57, v38
	v_dot4c_i32_i8_e32 v95, s57, v23
	v_dot4c_i32_i8_e32 v99, s57, v22
	v_dot4c_i32_i8_e32 v91, s57, v5
	v_dot4c_i32_i8_e32 v101, s57, v4
	v_dot4c_i32_i8_e32 v102, s57, v3
	v_dot4c_i32_i8_e32 v83, s57, v2
	s_add_i32 s57, s56, -11
	s_bitcmp0_b32 s57, 6
	s_cselect_b64 vcc, -1, 0
	v_cndmask_b32_e32 v2, v79, v78, vcc
	s_nop 0
	v_readlane_b32 s57, v2, s57
	s_lshl_b32 s57, s57, 10
	s_add_i32 s57, s57, 0x1000000
	s_nop 2
	buffer_load_dwordx4 v[2:5], v0, s[92:95], s57 offen
	s_add_i32 s57, s56, -10
	s_bitcmp0_b32 s57, 6
	s_cselect_b64 vcc, -1, 0
	v_cndmask_b32_e32 v22, v79, v78, vcc
	s_nop 0
	v_readlane_b32 s57, v22, s57
	s_lshl_b32 s57, s57, 10
	s_add_i32 s57, s57, 0x1000000
	s_nop 2
	buffer_load_dwordx4 v[22:25], v0, s[92:95], s57 offen
	s_add_i32 s57, s56, -9
	s_bitcmp0_b32 s57, 6
	s_cselect_b64 vcc, -1, 0
	v_cndmask_b32_e32 v38, v79, v78, vcc
	s_nop 0
	v_readlane_b32 s57, v38, s57
	s_lshl_b32 s57, s57, 10
	s_add_i32 s57, s57, 0x1000000
	s_nop 2
	buffer_load_dwordx4 v[38:41], v0, s[92:95], s57 offen
	s_add_i32 s57, s56, -8
	s_bitcmp0_b32 s57, 6
	s_cselect_b64 vcc, -1, 0
	v_cndmask_b32_e32 v54, v79, v78, vcc
	s_nop 0
	v_readlane_b32 s57, v54, s57
	s_lshl_b32 s57, s57, 10
	s_add_i32 s57, s57, 0x1000000
	s_nop 2
	buffer_load_dwordx4 v[54:57], v0, s[92:95], s57 offen
	s_add_i32 s57, s56, 0xffffff69
	s_waitcnt vmcnt(8)
	v_perm_b32 v112, v26, v10, s67
	v_perm_b32 v10, v26, v10, s68
	s_waitcnt vmcnt(6)
	v_perm_b32 v26, v58, v42, s67
	v_readlane_b32 s57, v111, s57
	v_perm_b32 v42, v58, v42, s68
	v_perm_b32 v58, v26, v112, s69
	v_perm_b32 v26, v26, v112, s33
	v_perm_b32 v112, v42, v10, s69
	v_perm_b32 v10, v42, v10, s33
	v_dot4c_i32_i8_e32 v74, s57, v26
	v_and_b32_e32 v26, 0xf0f0f0f0, v26
	v_dot4c_i32_i8_e32 v70, s57, v26
	v_and_b32_e32 v26, 0xf0f0f0f0, v112
	v_dot4c_i32_i8_e32 v76, s57, v10
	v_and_b32_e32 v10, 0xf0f0f0f0, v10
	v_and_b32_e32 v42, 0xf0f0f0f0, v58
	v_dot4c_i32_i8_e32 v72, s57, v26
	v_dot4c_i32_i8_e32 v73, s57, v10
	v_perm_b32 v10, v27, v11, s67
	v_perm_b32 v26, v59, v43, s67
	v_dot4c_i32_i8_e32 v69, s57, v42
	v_perm_b32 v11, v27, v11, s68
	v_perm_b32 v27, v59, v43, s68
	v_perm_b32 v42, v26, v10, s69
	v_perm_b32 v10, v26, v10, s33
	v_perm_b32 v26, v27, v11, s69
	v_dot4c_i32_i8_e32 v85, s57, v10
	v_and_b32_e32 v10, 0xf0f0f0f0, v10
	v_perm_b32 v11, v27, v11, s33
	v_dot4c_i32_i8_e32 v81, s57, v10
	v_and_b32_e32 v10, 0xf0f0f0f0, v26
	v_dot4c_i32_i8_e32 v82, s57, v10
	v_and_b32_e32 v10, 0xf0f0f0f0, v11
	v_and_b32_e32 v27, 0xf0f0f0f0, v42
	v_dot4c_i32_i8_e32 v94, s57, v11
	v_dot4c_i32_i8_e32 v84, s57, v10
	v_perm_b32 v10, v28, v12, s67
	v_perm_b32 v11, v28, v12, s68
	v_perm_b32 v12, v60, v44, s67
	v_dot4c_i32_i8_e32 v77, s57, v27
	v_dot4c_i32_i8_e32 v86, s57, v26
	v_perm_b32 v26, v60, v44, s68
	v_perm_b32 v27, v12, v10, s69
	v_perm_b32 v10, v12, v10, s33
	v_perm_b32 v12, v26, v11, s69
	v_dot4c_i32_i8_e32 v96, s57, v10
	v_and_b32_e32 v10, 0xf0f0f0f0, v10
	v_perm_b32 v11, v26, v11, s33
	v_dot4c_i32_i8_e32 v88, s57, v10
	v_and_b32_e32 v10, 0xf0f0f0f0, v12
	v_dot4c_i32_i8_e32 v89, s57, v10
	v_and_b32_e32 v10, 0xf0f0f0f0, v11
	v_and_b32_e32 v26, 0xf0f0f0f0, v27
	v_dot4c_i32_i8_e32 v97, s57, v12
	v_dot4c_i32_i8_e32 v90, s57, v10
	v_perm_b32 v10, v29, v13, s67
	v_perm_b32 v12, v61, v45, s67
	v_dot4c_i32_i8_e32 v87, s57, v26
	v_dot4c_i32_i8_e32 v98, s57, v11
	v_perm_b32 v11, v29, v13, s68
	v_perm_b32 v13, v61, v45, s68
	v_perm_b32 v26, v12, v10, s69
	v_perm_b32 v10, v12, v10, s33
	v_perm_b32 v12, v13, v11, s69
	v_dot4c_i32_i8_e32 v100, s57, v10
	v_and_b32_e32 v10, 0xf0f0f0f0, v10
	v_perm_b32 v11, v13, v11, s33
	v_dot4c_i32_i8_e32 v92, s57, v10
	v_and_b32_e32 v10, 0xf0f0f0f0, v12
	v_and_b32_e32 v13, 0xf0f0f0f0, v26
	v_dot4c_i32_i8_e32 v93, s57, v10
	v_and_b32_e32 v10, 0xf0f0f0f0, v11
	v_dot4c_i32_i8_e32 v66, s57, v58
	v_dot4c_i32_i8_e32 v75, s57, v112
	v_dot4c_i32_i8_e32 v80, s57, v42
	v_dot4c_i32_i8_e32 v95, s57, v27
	v_dot4c_i32_i8_e32 v99, s57, v26
	v_dot4c_i32_i8_e32 v91, s57, v13
	v_dot4c_i32_i8_e32 v101, s57, v12
	v_dot4c_i32_i8_e32 v102, s57, v11
	v_dot4c_i32_i8_e32 v83, s57, v10
	s_add_i32 s57, s56, -7
	s_bitcmp0_b32 s57, 6
	s_cselect_b64 vcc, -1, 0
	v_cndmask_b32_e32 v10, v79, v78, vcc
	s_nop 0
	v_readlane_b32 s57, v10, s57
	s_lshl_b32 s57, s57, 10
	s_add_i32 s57, s57, 0x1000000
	s_nop 2
	buffer_load_dwordx4 v[10:13], v0, s[92:95], s57 offen
	s_add_i32 s57, s56, -6
	s_bitcmp0_b32 s57, 6
	s_cselect_b64 vcc, -1, 0
	v_cndmask_b32_e32 v26, v79, v78, vcc
	s_nop 0
	v_readlane_b32 s57, v26, s57
	s_lshl_b32 s57, s57, 10
	s_add_i32 s57, s57, 0x1000000
	s_nop 2
	buffer_load_dwordx4 v[26:29], v0, s[92:95], s57 offen
	s_add_i32 s57, s56, -5
	s_bitcmp0_b32 s57, 6
	s_cselect_b64 vcc, -1, 0
	v_cndmask_b32_e32 v42, v79, v78, vcc
	s_nop 0
	v_readlane_b32 s57, v42, s57
	s_lshl_b32 s57, s57, 10
	s_add_i32 s57, s57, 0x1000000
	s_nop 2
	buffer_load_dwordx4 v[42:45], v0, s[92:95], s57 offen
	s_add_i32 s57, s56, -4
	s_bitcmp0_b32 s57, 6
	s_cselect_b64 vcc, -1, 0
	v_cndmask_b32_e32 v58, v79, v78, vcc
	s_nop 0
	v_readlane_b32 s57, v58, s57
	s_lshl_b32 s57, s57, 10
	s_add_i32 s57, s57, 0x1000000
	s_nop 2
	buffer_load_dwordx4 v[58:61], v0, s[92:95], s57 offen
	s_add_i32 s57, s56, 0xffffff6d
	s_waitcnt vmcnt(8)
; __device__ __forceinline__ int shl_i(int v, int from_lane) { return __builtin_amdgcn_ds_bpermute(from_lane << 2, v); }
;     ...
;         const int pk0 = (q0 & 0xFF) | ((shl_i(q0, lane + 1) & 0xFF) << 8) | ((shl_i(q0, lane + 2) & 0xFF) << 16) | (shl_i(q0, lane + 3) << 24);
;         const int pk1 = (q1 & 0xFF) | ((shl_i(q1, lane + 1) & 0xFF) << 8) | ((shl_i(q1, lane + 2) & 0xFF) << 16) | (shl_i(q1, lane + 3) << 24);
	v_perm_b32 v112, v34, v18, s67
	v_perm_b32 v18, v34, v18, s68
	s_waitcnt vmcnt(6)
	v_perm_b32 v34, v62, v50, s67
	v_readlane_b32 s57, v111, s57
	v_perm_b32 v50, v62, v50, s68
	v_perm_b32 v62, v34, v112, s69
	v_perm_b32 v34, v34, v112, s33
	v_perm_b32 v112, v50, v18, s69
	v_perm_b32 v18, v50, v18, s33
	v_dot4c_i32_i8_e32 v74, s57, v34
	v_and_b32_e32 v34, 0xf0f0f0f0, v34
	v_dot4c_i32_i8_e32 v70, s57, v34
	v_and_b32_e32 v34, 0xf0f0f0f0, v112
	v_dot4c_i32_i8_e32 v76, s57, v18
	v_and_b32_e32 v18, 0xf0f0f0f0, v18
	v_and_b32_e32 v50, 0xf0f0f0f0, v62
	v_dot4c_i32_i8_e32 v72, s57, v34
	v_dot4c_i32_i8_e32 v73, s57, v18
	v_perm_b32 v18, v35, v19, s67
	v_perm_b32 v34, v63, v51, s67
	v_dot4c_i32_i8_e32 v69, s57, v50
	v_perm_b32 v19, v35, v19, s68
	v_perm_b32 v35, v63, v51, s68
	v_perm_b32 v50, v34, v18, s69
	v_perm_b32 v18, v34, v18, s33
	v_perm_b32 v34, v35, v19, s69
	v_dot4c_i32_i8_e32 v85, s57, v18
	v_and_b32_e32 v18, 0xf0f0f0f0, v18
	v_perm_b32 v19, v35, v19, s33
	v_dot4c_i32_i8_e32 v81, s57, v18
	v_and_b32_e32 v18, 0xf0f0f0f0, v34
	v_dot4c_i32_i8_e32 v82, s57, v18
	v_and_b32_e32 v18, 0xf0f0f0f0, v19
	v_and_b32_e32 v35, 0xf0f0f0f0, v50
	v_dot4c_i32_i8_e32 v94, s57, v19
	v_dot4c_i32_i8_e32 v84, s57, v18
	v_perm_b32 v18, v36, v20, s67
	v_perm_b32 v19, v36, v20, s68
	v_perm_b32 v20, v64, v52, s67
	v_dot4c_i32_i8_e32 v77, s57, v35
	v_dot4c_i32_i8_e32 v86, s57, v34
	v_perm_b32 v34, v64, v52, s68
	v_perm_b32 v35, v20, v18, s69
	v_perm_b32 v18, v20, v18, s33
	v_perm_b32 v20, v34, v19, s69
	v_dot4c_i32_i8_e32 v96, s57, v18
	v_and_b32_e32 v18, 0xf0f0f0f0, v18
	v_perm_b32 v19, v34, v19, s33
	v_dot4c_i32_i8_e32 v88, s57, v18
	v_and_b32_e32 v18, 0xf0f0f0f0, v20
	v_dot4c_i32_i8_e32 v89, s57, v18
	v_and_b32_e32 v18, 0xf0f0f0f0, v19
	v_and_b32_e32 v34, 0xf0f0f0f0, v35
	v_dot4c_i32_i8_e32 v97, s57, v20
	v_dot4c_i32_i8_e32 v90, s57, v18
	v_perm_b32 v18, v37, v21, s67
	v_perm_b32 v20, v65, v53, s67
	v_dot4c_i32_i8_e32 v87, s57, v34
	v_dot4c_i32_i8_e32 v98, s57, v19
	v_perm_b32 v19, v37, v21, s68
	v_perm_b32 v21, v65, v53, s68
	v_perm_b32 v34, v20, v18, s69
	v_perm_b32 v18, v20, v18, s33
	v_perm_b32 v20, v21, v19, s69
	v_dot4c_i32_i8_e32 v100, s57, v18
	v_and_b32_e32 v18, 0xf0f0f0f0, v18
	v_perm_b32 v19, v21, v19, s33
	v_dot4c_i32_i8_e32 v92, s57, v18
	v_and_b32_e32 v18, 0xf0f0f0f0, v20
	v_and_b32_e32 v21, 0xf0f0f0f0, v34
	v_dot4c_i32_i8_e32 v93, s57, v18
	v_and_b32_e32 v18, 0xf0f0f0f0, v19
	v_dot4c_i32_i8_e32 v66, s57, v62
	v_dot4c_i32_i8_e32 v75, s57, v112
	v_dot4c_i32_i8_e32 v80, s57, v50
	v_dot4c_i32_i8_e32 v95, s57, v35
	v_dot4c_i32_i8_e32 v99, s57, v34
	v_dot4c_i32_i8_e32 v91, s57, v21
	v_dot4c_i32_i8_e32 v101, s57, v20
	v_dot4c_i32_i8_e32 v102, s57, v19
	v_dot4c_i32_i8_e32 v83, s57, v18
	s_add_i32 s57, s56, -3
	s_bitcmp0_b32 s57, 6
	s_cselect_b64 vcc, -1, 0
	v_cndmask_b32_e32 v18, v79, v78, vcc
	s_nop 0
	v_readlane_b32 s57, v18, s57
	s_lshl_b32 s57, s57, 10
	s_add_i32 s57, s57, 0x1000000
	s_nop 2
	buffer_load_dwordx4 v[18:21], v0, s[92:95], s57 offen
	s_add_i32 s57, s56, -2
	s_bitcmp0_b32 s57, 6
	s_cselect_b64 vcc, -1, 0
	v_cndmask_b32_e32 v34, v79, v78, vcc
	s_nop 0
	v_readlane_b32 s57, v34, s57
	s_lshl_b32 s57, s57, 10
	s_add_i32 s57, s57, 0x1000000
	s_nop 2
	buffer_load_dwordx4 v[34:37], v0, s[92:95], s57 offen
	s_add_i32 s57, s56, -1
	s_bitcmp0_b32 s57, 6
	s_cselect_b64 vcc, -1, 0
	v_cndmask_b32_e32 v50, v79, v78, vcc
	s_nop 0
	v_readlane_b32 s57, v50, s57
	s_lshl_b32 s57, s57, 10
	s_add_i32 s57, s57, 0x1000000
	s_bitcmp0_b32 s56, 6
	s_cselect_b64 vcc, -1, 0
	v_cndmask_b32_e32 v62, v79, v78, vcc
	buffer_load_dwordx4 v[50:53], v0, s[92:95], s57 offen
	v_readlane_b32 s57, v62, s56
	s_lshl_b32 s57, s57, 10
	s_add_i32 s57, s57, 0x1000000
	s_nop 2
	buffer_load_dwordx4 v[62:65], v0, s[92:95], s57 offen
	s_add_i32 s56, s56, 16
	s_cmpk_lg_i32 s56, 0xdf
	s_cbranch_scc1 .LBB0_1423
	v_min_u32_e32 v111, v105, v106
	v_max_u32_e32 v105, v105, v106
	v_cndmask_b32_e64 v200, v105, v111, s[6:7]
	v_lshlrev_b32_e32 v105, 8, v108
	v_lshlrev_b32_e32 v106, 16, v109
	s_mov_b32 s56, 0xc0c0500
	v_lshlrev_b32_e32 v108, 24, v110
	v_perm_b32 v105, v105, v107, s56
	v_and_b32_e32 v106, 0xff0000, v106
	v_lshrrev_b32_e32 v199, 16, v200
	v_or3_b32 v105, v105, v106, v108
	s_mov_b32 s62, 0
	s_movk_i32 s63, 0xdf
	s_mov_b32 s90, 0x1be0000
	s_cmp_eq_u32 s101, 0
	s_cbranch_scc1 .Lnb_1425
	s_barrier
.Lnb_1425:
.LBB0_1425:
	s_add_i32 s56, s63, 0xffffff21
	s_waitcnt vmcnt(8)
	v_perm_b32 v106, v14, v6, s67
	v_perm_b32 v6, v14, v6, s68
	s_waitcnt vmcnt(6)
	v_perm_b32 v14, v46, v30, s67
	v_readlane_b32 s56, v105, s56
	v_perm_b32 v30, v46, v30, s68
	v_perm_b32 v46, v14, v106, s69
	v_perm_b32 v14, v14, v106, s33
	v_perm_b32 v106, v30, v6, s69
	v_perm_b32 v6, v30, v6, s33
	v_dot4c_i32_i8_e32 v74, s56, v14
	v_and_b32_e32 v14, 0xf0f0f0f0, v14
	v_dot4c_i32_i8_e32 v70, s56, v14
	v_and_b32_e32 v14, 0xf0f0f0f0, v106
	v_dot4c_i32_i8_e32 v76, s56, v6
	v_and_b32_e32 v6, 0xf0f0f0f0, v6
	v_and_b32_e32 v30, 0xf0f0f0f0, v46
	v_dot4c_i32_i8_e32 v72, s56, v14
	v_dot4c_i32_i8_e32 v73, s56, v6
	v_perm_b32 v6, v15, v7, s67
	v_perm_b32 v14, v47, v31, s67
	v_dot4c_i32_i8_e32 v69, s56, v30
	v_perm_b32 v7, v15, v7, s68
	v_perm_b32 v15, v47, v31, s68
	v_perm_b32 v30, v14, v6, s69
	v_perm_b32 v6, v14, v6, s33
	v_perm_b32 v14, v15, v7, s69
	v_dot4c_i32_i8_e32 v85, s56, v6
	v_and_b32_e32 v6, 0xf0f0f0f0, v6
	v_perm_b32 v7, v15, v7, s33
	v_dot4c_i32_i8_e32 v81, s56, v6
	v_and_b32_e32 v6, 0xf0f0f0f0, v14
	v_dot4c_i32_i8_e32 v82, s56, v6
	v_and_b32_e32 v6, 0xf0f0f0f0, v7
	v_and_b32_e32 v15, 0xf0f0f0f0, v30
	v_dot4c_i32_i8_e32 v94, s56, v7
	v_dot4c_i32_i8_e32 v84, s56, v6
	v_perm_b32 v6, v16, v8, s67
	v_perm_b32 v7, v16, v8, s68
	v_perm_b32 v8, v48, v32, s67
	v_dot4c_i32_i8_e32 v77, s56, v15
	v_dot4c_i32_i8_e32 v86, s56, v14
	v_perm_b32 v14, v48, v32, s68
	v_perm_b32 v15, v8, v6, s69
	v_perm_b32 v6, v8, v6, s33
	v_perm_b32 v8, v14, v7, s69
	v_dot4c_i32_i8_e32 v96, s56, v6
	v_and_b32_e32 v6, 0xf0f0f0f0, v6
	v_perm_b32 v7, v14, v7, s33
	v_dot4c_i32_i8_e32 v88, s56, v6
	v_and_b32_e32 v6, 0xf0f0f0f0, v8
	v_dot4c_i32_i8_e32 v89, s56, v6
	v_and_b32_e32 v6, 0xf0f0f0f0, v7
	v_and_b32_e32 v14, 0xf0f0f0f0, v15
	v_dot4c_i32_i8_e32 v97, s56, v8
	v_dot4c_i32_i8_e32 v90, s56, v6
	v_perm_b32 v6, v17, v9, s67
	v_perm_b32 v8, v49, v33, s67
	v_dot4c_i32_i8_e32 v87, s56, v14
	v_dot4c_i32_i8_e32 v98, s56, v7
	v_perm_b32 v7, v17, v9, s68
	v_perm_b32 v9, v49, v33, s68
	v_perm_b32 v14, v8, v6, s69
	v_perm_b32 v6, v8, v6, s33
	v_perm_b32 v8, v9, v7, s69
	v_dot4c_i32_i8_e32 v100, s56, v6
	v_and_b32_e32 v6, 0xf0f0f0f0, v6
	s_add_i32 s91, s63, -15
	v_perm_b32 v7, v9, v7, s33
	v_dot4c_i32_i8_e32 v92, s56, v6
	v_and_b32_e32 v6, 0xf0f0f0f0, v8
	s_cmp_gt_u32 s62, 2
	v_and_b32_e32 v9, 0xf0f0f0f0, v14
	v_dot4c_i32_i8_e32 v93, s56, v6
	v_and_b32_e32 v6, 0xf0f0f0f0, v7
	s_cselect_b64 vcc, -1, 0
	s_bitcmp0_b32 s91, 6
	v_dot4c_i32_i8_e32 v66, s56, v46
	v_dot4c_i32_i8_e32 v75, s56, v106
	v_dot4c_i32_i8_e32 v80, s56, v30
	v_dot4c_i32_i8_e32 v95, s56, v15
	v_dot4c_i32_i8_e32 v99, s56, v14
	v_dot4c_i32_i8_e32 v91, s56, v9
	v_dot4c_i32_i8_e32 v101, s56, v8
	v_dot4c_i32_i8_e32 v102, s56, v7
	v_dot4c_i32_i8_e32 v83, s56, v6
	s_cselect_b64 s[56:57], -1, 0
	v_cndmask_b32_e64 v6, v79, v78, s[56:57]
	v_cndmask_b32_e32 v6, v6, v199, vcc
	s_add_i32 s57, s90, 0xffe20000
	v_readlane_b32 s56, v6, s91
	s_lshl_b32 s56, s56, 10
	s_and_b32 s57, s57, 0x1000000
	s_add_i32 s56, s56, s57
	s_add_i32 s91, s63, -14
	s_bitcmp0_b32 s91, 6
	buffer_load_dwordx4 v[6:9], v0, s[92:95], s56 offen
	s_cselect_b64 s[56:57], -1, 0
	v_cndmask_b32_e64 v14, v79, v78, s[56:57]
	v_cndmask_b32_e32 v14, v14, v199, vcc
	s_add_i32 s57, s90, 0xffe40000
	v_readlane_b32 s56, v14, s91
	s_lshl_b32 s56, s56, 10
	s_and_b32 s57, s57, 0x1000000
	s_add_i32 s56, s56, s57
	s_add_i32 s91, s63, -13
	s_bitcmp0_b32 s91, 6
	buffer_load_dwordx4 v[14:17], v0, s[92:95], s56 offen
	s_cselect_b64 s[56:57], -1, 0
	v_cndmask_b32_e64 v30, v79, v78, s[56:57]
	v_cndmask_b32_e32 v30, v30, v199, vcc
	s_add_i32 s57, s90, 0xffe60000
	v_readlane_b32 s56, v30, s91
	s_lshl_b32 s56, s56, 10
	s_and_b32 s57, s57, 0x1000000
	s_add_i32 s56, s56, s57
	s_add_i32 s91, s63, -12
	s_bitcmp0_b32 s91, 6
	buffer_load_dwordx4 v[30:33], v0, s[92:95], s56 offen
	s_cselect_b64 s[56:57], -1, 0
	v_cndmask_b32_e64 v46, v79, v78, s[56:57]
	v_cndmask_b32_e32 v46, v46, v199, vcc
	s_add_i32 s57, s90, 0xffe80000
	v_readlane_b32 s56, v46, s91
	s_lshl_b32 s56, s56, 10
	s_and_b32 s57, s57, 0x1000000
	s_add_i32 s56, s56, s57
	s_nop 1
	buffer_load_dwordx4 v[46:49], v0, s[92:95], s56 offen
	s_add_i32 s56, s63, 0xffffff25
	s_waitcnt vmcnt(8)
	v_perm_b32 v106, v22, v2, s67
	v_perm_b32 v2, v22, v2, s68
	s_waitcnt vmcnt(6)
	v_perm_b32 v22, v54, v38, s67
	v_readlane_b32 s56, v105, s56
	v_perm_b32 v38, v54, v38, s68
	v_perm_b32 v54, v22, v106, s69
	v_perm_b32 v22, v22, v106, s33
	v_perm_b32 v106, v38, v2, s69
	v_perm_b32 v2, v38, v2, s33
	v_dot4c_i32_i8_e32 v74, s56, v22
	v_and_b32_e32 v22, 0xf0f0f0f0, v22
	v_dot4c_i32_i8_e32 v70, s56, v22
	v_and_b32_e32 v22, 0xf0f0f0f0, v106
	v_dot4c_i32_i8_e32 v76, s56, v2
	v_and_b32_e32 v2, 0xf0f0f0f0, v2
	v_and_b32_e32 v38, 0xf0f0f0f0, v54
	v_dot4c_i32_i8_e32 v72, s56, v22
	v_dot4c_i32_i8_e32 v73, s56, v2
	v_perm_b32 v2, v23, v3, s67
	v_perm_b32 v22, v55, v39, s67
	v_dot4c_i32_i8_e32 v69, s56, v38
	v_perm_b32 v3, v23, v3, s68
	v_perm_b32 v23, v55, v39, s68
	v_perm_b32 v38, v22, v2, s69
	v_perm_b32 v2, v22, v2, s33
	v_perm_b32 v22, v23, v3, s69
	v_dot4c_i32_i8_e32 v85, s56, v2
	v_and_b32_e32 v2, 0xf0f0f0f0, v2
	v_perm_b32 v3, v23, v3, s33
	v_dot4c_i32_i8_e32 v81, s56, v2
	v_and_b32_e32 v2, 0xf0f0f0f0, v22
	v_dot4c_i32_i8_e32 v82, s56, v2
	v_and_b32_e32 v2, 0xf0f0f0f0, v3
	v_and_b32_e32 v23, 0xf0f0f0f0, v38
	v_dot4c_i32_i8_e32 v94, s56, v3
	v_dot4c_i32_i8_e32 v84, s56, v2
	v_perm_b32 v2, v24, v4, s67
	v_perm_b32 v3, v24, v4, s68
	v_perm_b32 v4, v56, v40, s67
	v_dot4c_i32_i8_e32 v77, s56, v23
	v_dot4c_i32_i8_e32 v86, s56, v22
	v_perm_b32 v22, v56, v40, s68
	v_perm_b32 v23, v4, v2, s69
	v_perm_b32 v2, v4, v2, s33
	v_perm_b32 v4, v22, v3, s69
	v_dot4c_i32_i8_e32 v96, s56, v2
	v_and_b32_e32 v2, 0xf0f0f0f0, v2
	v_perm_b32 v3, v22, v3, s33
	v_dot4c_i32_i8_e32 v88, s56, v2
	v_and_b32_e32 v2, 0xf0f0f0f0, v4
	v_dot4c_i32_i8_e32 v89, s56, v2
	v_and_b32_e32 v2, 0xf0f0f0f0, v3
	v_and_b32_e32 v22, 0xf0f0f0f0, v23
	v_dot4c_i32_i8_e32 v97, s56, v4
	v_dot4c_i32_i8_e32 v90, s56, v2
	v_perm_b32 v2, v25, v5, s67
	v_perm_b32 v4, v57, v41, s67
	v_dot4c_i32_i8_e32 v87, s56, v22
	v_dot4c_i32_i8_e32 v98, s56, v3
	v_perm_b32 v3, v25, v5, s68
	v_perm_b32 v5, v57, v41, s68
	v_perm_b32 v22, v4, v2, s69
	v_perm_b32 v2, v4, v2, s33
	v_perm_b32 v4, v5, v3, s69
	v_dot4c_i32_i8_e32 v100, s56, v2
	v_and_b32_e32 v2, 0xf0f0f0f0, v2
	v_perm_b32 v3, v5, v3, s33
	v_dot4c_i32_i8_e32 v92, s56, v2
	v_and_b32_e32 v2, 0xf0f0f0f0, v4
	s_add_i32 s91, s63, -11
	v_and_b32_e32 v5, 0xf0f0f0f0, v22
	v_dot4c_i32_i8_e32 v93, s56, v2
	v_and_b32_e32 v2, 0xf0f0f0f0, v3
	s_bitcmp0_b32 s91, 6
	v_dot4c_i32_i8_e32 v66, s56, v54
	v_dot4c_i32_i8_e32 v75, s56, v106
	v_dot4c_i32_i8_e32 v80, s56, v38
	v_dot4c_i32_i8_e32 v95, s56, v23
	v_dot4c_i32_i8_e32 v99, s56, v22
	v_dot4c_i32_i8_e32 v91, s56, v5
	v_dot4c_i32_i8_e32 v101, s56, v4
	v_dot4c_i32_i8_e32 v102, s56, v3
	v_dot4c_i32_i8_e32 v83, s56, v2
	s_cselect_b64 s[56:57], -1, 0
	v_cndmask_b32_e64 v2, v79, v78, s[56:57]
	v_cndmask_b32_e32 v2, v2, v199, vcc
	s_add_i32 s57, s90, 0xffea0000
	v_readlane_b32 s56, v2, s91
	s_lshl_b32 s56, s56, 10
	s_and_b32 s57, s57, 0x1000000
	s_add_i32 s56, s56, s57
	s_add_i32 s91, s63, -10
	s_bitcmp0_b32 s91, 6
	buffer_load_dwordx4 v[2:5], v0, s[92:95], s56 offen
	s_cselect_b64 s[56:57], -1, 0
	v_cndmask_b32_e64 v22, v79, v78, s[56:57]
	v_cndmask_b32_e32 v22, v22, v199, vcc
	s_add_i32 s57, s90, 0xffec0000
	v_readlane_b32 s56, v22, s91
	s_lshl_b32 s56, s56, 10
	s_and_b32 s57, s57, 0x1000000
	s_add_i32 s56, s56, s57
	s_add_i32 s91, s63, -9
	s_bitcmp0_b32 s91, 6
	buffer_load_dwordx4 v[22:25], v0, s[92:95], s56 offen
	s_cselect_b64 s[56:57], -1, 0
	v_cndmask_b32_e64 v38, v79, v78, s[56:57]
	v_cndmask_b32_e32 v38, v38, v199, vcc
	s_add_i32 s57, s90, 0xffee0000
	v_readlane_b32 s56, v38, s91
	s_lshl_b32 s56, s56, 10
	s_and_b32 s57, s57, 0x1000000
	s_add_i32 s56, s56, s57
	s_add_i32 s91, s63, -8
	s_bitcmp0_b32 s91, 6
	buffer_load_dwordx4 v[38:41], v0, s[92:95], s56 offen
	s_cselect_b64 s[56:57], -1, 0
	v_cndmask_b32_e64 v54, v79, v78, s[56:57]
	v_cndmask_b32_e32 v54, v54, v199, vcc
	s_add_i32 s57, s90, 0xfff00000
	v_readlane_b32 s56, v54, s91
	s_lshl_b32 s56, s56, 10
	s_and_b32 s57, s57, 0x1000000
	s_add_i32 s56, s56, s57
	s_nop 1
	buffer_load_dwordx4 v[54:57], v0, s[92:95], s56 offen
	s_add_i32 s56, s63, 0xffffff29
	s_waitcnt vmcnt(8)
	v_perm_b32 v106, v26, v10, s67
	v_perm_b32 v10, v26, v10, s68
	s_waitcnt vmcnt(6)
	v_perm_b32 v26, v58, v42, s67
	v_readlane_b32 s56, v105, s56
	v_perm_b32 v42, v58, v42, s68
	v_perm_b32 v58, v26, v106, s69
	v_perm_b32 v26, v26, v106, s33
	v_perm_b32 v106, v42, v10, s69
	v_perm_b32 v10, v42, v10, s33
	v_dot4c_i32_i8_e32 v74, s56, v26
	v_and_b32_e32 v26, 0xf0f0f0f0, v26
	v_dot4c_i32_i8_e32 v70, s56, v26
	v_and_b32_e32 v26, 0xf0f0f0f0, v106
	v_dot4c_i32_i8_e32 v76, s56, v10
	v_and_b32_e32 v10, 0xf0f0f0f0, v10
	v_and_b32_e32 v42, 0xf0f0f0f0, v58
	v_dot4c_i32_i8_e32 v72, s56, v26
	v_dot4c_i32_i8_e32 v73, s56, v10
	v_perm_b32 v10, v27, v11, s67
	v_perm_b32 v26, v59, v43, s67
	v_dot4c_i32_i8_e32 v69, s56, v42
	v_perm_b32 v11, v27, v11, s68
	v_perm_b32 v27, v59, v43, s68
	v_perm_b32 v42, v26, v10, s69
	v_perm_b32 v10, v26, v10, s33
	v_perm_b32 v26, v27, v11, s69
	v_dot4c_i32_i8_e32 v85, s56, v10
	v_and_b32_e32 v10, 0xf0f0f0f0, v10
	v_perm_b32 v11, v27, v11, s33
	v_dot4c_i32_i8_e32 v81, s56, v10
	v_and_b32_e32 v10, 0xf0f0f0f0, v26
	v_dot4c_i32_i8_e32 v82, s56, v10
	v_and_b32_e32 v10, 0xf0f0f0f0, v11
	v_and_b32_e32 v27, 0xf0f0f0f0, v42
	v_dot4c_i32_i8_e32 v94, s56, v11
	v_dot4c_i32_i8_e32 v84, s56, v10
	v_perm_b32 v10, v28, v12, s67
	v_perm_b32 v11, v28, v12, s68
	v_perm_b32 v12, v60, v44, s67
	v_dot4c_i32_i8_e32 v77, s56, v27
	v_dot4c_i32_i8_e32 v86, s56, v26
	v_perm_b32 v26, v60, v44, s68
	v_perm_b32 v27, v12, v10, s69
	v_perm_b32 v10, v12, v10, s33
	v_perm_b32 v12, v26, v11, s69
	v_dot4c_i32_i8_e32 v96, s56, v10
	v_and_b32_e32 v10, 0xf0f0f0f0, v10
	v_perm_b32 v11, v26, v11, s33
	v_dot4c_i32_i8_e32 v88, s56, v10
	v_and_b32_e32 v10, 0xf0f0f0f0, v12
	v_dot4c_i32_i8_e32 v89, s56, v10
	v_and_b32_e32 v10, 0xf0f0f0f0, v11
	v_and_b32_e32 v26, 0xf0f0f0f0, v27
	v_dot4c_i32_i8_e32 v97, s56, v12
	v_dot4c_i32_i8_e32 v90, s56, v10
	v_perm_b32 v10, v29, v13, s67
	v_perm_b32 v12, v61, v45, s67
	v_dot4c_i32_i8_e32 v87, s56, v26
	v_dot4c_i32_i8_e32 v98, s56, v11
	v_perm_b32 v11, v29, v13, s68
	v_perm_b32 v13, v61, v45, s68
	v_perm_b32 v26, v12, v10, s69
	v_perm_b32 v10, v12, v10, s33
	v_perm_b32 v12, v13, v11, s69
	v_dot4c_i32_i8_e32 v100, s56, v10
	v_and_b32_e32 v10, 0xf0f0f0f0, v10
	v_perm_b32 v11, v13, v11, s33
	v_dot4c_i32_i8_e32 v92, s56, v10
	v_and_b32_e32 v10, 0xf0f0f0f0, v12
	s_add_i32 s91, s63, -7
	v_and_b32_e32 v13, 0xf0f0f0f0, v26
	v_dot4c_i32_i8_e32 v93, s56, v10
	v_and_b32_e32 v10, 0xf0f0f0f0, v11
	s_bitcmp0_b32 s91, 6
	v_dot4c_i32_i8_e32 v66, s56, v58
	v_dot4c_i32_i8_e32 v75, s56, v106
	v_dot4c_i32_i8_e32 v80, s56, v42
	v_dot4c_i32_i8_e32 v95, s56, v27
	v_dot4c_i32_i8_e32 v99, s56, v26
	v_dot4c_i32_i8_e32 v91, s56, v13
	v_dot4c_i32_i8_e32 v101, s56, v12
	v_dot4c_i32_i8_e32 v102, s56, v11
	v_dot4c_i32_i8_e32 v83, s56, v10
	s_cselect_b64 s[56:57], -1, 0
	v_cndmask_b32_e64 v10, v79, v78, s[56:57]
	v_cndmask_b32_e32 v10, v10, v199, vcc
	s_add_i32 s57, s90, 0xfff20000
	v_readlane_b32 s56, v10, s91
	s_lshl_b32 s56, s56, 10
	s_and_b32 s57, s57, 0x1000000
	s_add_i32 s56, s56, s57
	s_add_i32 s91, s63, -6
	s_bitcmp0_b32 s91, 6
	buffer_load_dwordx4 v[10:13], v0, s[92:95], s56 offen
	s_cselect_b64 s[56:57], -1, 0
	v_cndmask_b32_e64 v26, v79, v78, s[56:57]
	v_cndmask_b32_e32 v26, v26, v199, vcc
	s_add_i32 s57, s90, 0xfff40000
	v_readlane_b32 s56, v26, s91
	s_lshl_b32 s56, s56, 10
	s_and_b32 s57, s57, 0x1000000
	s_add_i32 s56, s56, s57
	s_add_i32 s91, s63, -5
	s_bitcmp0_b32 s91, 6
	buffer_load_dwordx4 v[26:29], v0, s[92:95], s56 offen
	s_cselect_b64 s[56:57], -1, 0
	v_cndmask_b32_e64 v42, v79, v78, s[56:57]
	v_cndmask_b32_e32 v42, v42, v199, vcc
	s_add_i32 s57, s90, 0xfff60000
	v_readlane_b32 s56, v42, s91
	s_lshl_b32 s56, s56, 10
	s_and_b32 s57, s57, 0x1000000
	s_add_i32 s56, s56, s57
	s_add_i32 s91, s63, -4
	s_bitcmp0_b32 s91, 6
	buffer_load_dwordx4 v[42:45], v0, s[92:95], s56 offen
	s_cselect_b64 s[56:57], -1, 0
	v_cndmask_b32_e64 v58, v79, v78, s[56:57]
	v_cndmask_b32_e32 v58, v58, v199, vcc
	s_add_i32 s57, s90, 0xfff80000
	v_readlane_b32 s56, v58, s91
	s_lshl_b32 s56, s56, 10
	s_and_b32 s57, s57, 0x1000000
	s_add_i32 s56, s56, s57
	s_nop 1
	buffer_load_dwordx4 v[58:61], v0, s[92:95], s56 offen
	s_add_i32 s56, s63, 0xffffff2d
	s_waitcnt vmcnt(8)
	v_perm_b32 v106, v34, v18, s67
	v_perm_b32 v18, v34, v18, s68
	s_waitcnt vmcnt(6)
	v_perm_b32 v34, v62, v50, s67
	v_readlane_b32 s56, v105, s56
	v_perm_b32 v50, v62, v50, s68
	v_perm_b32 v62, v34, v106, s69
	v_perm_b32 v34, v34, v106, s33
	v_perm_b32 v106, v50, v18, s69
	v_perm_b32 v18, v50, v18, s33
	v_dot4c_i32_i8_e32 v74, s56, v34
	v_and_b32_e32 v34, 0xf0f0f0f0, v34
	v_dot4c_i32_i8_e32 v70, s56, v34
	v_and_b32_e32 v34, 0xf0f0f0f0, v106
	v_dot4c_i32_i8_e32 v76, s56, v18
	v_and_b32_e32 v18, 0xf0f0f0f0, v18
	v_and_b32_e32 v50, 0xf0f0f0f0, v62
	v_dot4c_i32_i8_e32 v72, s56, v34
	v_dot4c_i32_i8_e32 v73, s56, v18
	v_perm_b32 v18, v35, v19, s67
	v_perm_b32 v34, v63, v51, s67
	v_dot4c_i32_i8_e32 v69, s56, v50
	v_perm_b32 v19, v35, v19, s68
	v_perm_b32 v35, v63, v51, s68
	v_perm_b32 v50, v34, v18, s69
	v_perm_b32 v18, v34, v18, s33
	v_perm_b32 v34, v35, v19, s69
	v_dot4c_i32_i8_e32 v85, s56, v18
	v_and_b32_e32 v18, 0xf0f0f0f0, v18
	v_perm_b32 v19, v35, v19, s33
	v_dot4c_i32_i8_e32 v81, s56, v18
	v_and_b32_e32 v18, 0xf0f0f0f0, v34
	v_dot4c_i32_i8_e32 v82, s56, v18
	v_and_b32_e32 v18, 0xf0f0f0f0, v19
	v_and_b32_e32 v35, 0xf0f0f0f0, v50
	v_dot4c_i32_i8_e32 v94, s56, v19
	v_dot4c_i32_i8_e32 v84, s56, v18
	v_perm_b32 v18, v36, v20, s67
	v_perm_b32 v19, v36, v20, s68
	v_perm_b32 v20, v64, v52, s67
	v_dot4c_i32_i8_e32 v77, s56, v35
	v_dot4c_i32_i8_e32 v86, s56, v34
	v_perm_b32 v34, v64, v52, s68
	v_perm_b32 v35, v20, v18, s69
	v_perm_b32 v18, v20, v18, s33
	v_perm_b32 v20, v34, v19, s69
	v_dot4c_i32_i8_e32 v96, s56, v18
	v_and_b32_e32 v18, 0xf0f0f0f0, v18
	v_perm_b32 v19, v34, v19, s33
	v_dot4c_i32_i8_e32 v88, s56, v18
	v_and_b32_e32 v18, 0xf0f0f0f0, v20
	v_dot4c_i32_i8_e32 v89, s56, v18
	v_and_b32_e32 v18, 0xf0f0f0f0, v19
	v_and_b32_e32 v34, 0xf0f0f0f0, v35
	v_dot4c_i32_i8_e32 v97, s56, v20
	v_dot4c_i32_i8_e32 v90, s56, v18
	v_perm_b32 v18, v37, v21, s67
	v_perm_b32 v20, v65, v53, s67
	v_dot4c_i32_i8_e32 v87, s56, v34
	v_dot4c_i32_i8_e32 v98, s56, v19
	v_perm_b32 v19, v37, v21, s68
	v_perm_b32 v21, v65, v53, s68
	v_perm_b32 v34, v20, v18, s69
	v_perm_b32 v18, v20, v18, s33
	v_perm_b32 v20, v21, v19, s69
	v_dot4c_i32_i8_e32 v100, s56, v18
	v_and_b32_e32 v18, 0xf0f0f0f0, v18
	v_perm_b32 v19, v21, v19, s33
	v_dot4c_i32_i8_e32 v92, s56, v18
	v_and_b32_e32 v18, 0xf0f0f0f0, v20
	s_add_i32 s91, s63, -3
	v_and_b32_e32 v21, 0xf0f0f0f0, v34
	v_dot4c_i32_i8_e32 v93, s56, v18
	v_and_b32_e32 v18, 0xf0f0f0f0, v19
	s_bitcmp0_b32 s91, 6
	v_dot4c_i32_i8_e32 v66, s56, v62
	v_dot4c_i32_i8_e32 v75, s56, v106
	v_dot4c_i32_i8_e32 v80, s56, v50
	v_dot4c_i32_i8_e32 v95, s56, v35
	v_dot4c_i32_i8_e32 v99, s56, v34
	v_dot4c_i32_i8_e32 v91, s56, v21
	v_dot4c_i32_i8_e32 v101, s56, v20
	v_dot4c_i32_i8_e32 v102, s56, v19
	v_dot4c_i32_i8_e32 v83, s56, v18
	s_cselect_b64 s[56:57], -1, 0
	v_cndmask_b32_e64 v18, v79, v78, s[56:57]
	v_cndmask_b32_e32 v18, v18, v199, vcc
	s_add_i32 s57, s90, 0xfffa0000
	v_readlane_b32 s56, v18, s91
	s_lshl_b32 s56, s56, 10
	s_and_b32 s57, s57, 0x1000000
	s_add_i32 s56, s56, s57
	s_add_i32 s91, s63, -2
	s_bitcmp0_b32 s91, 6
	buffer_load_dwordx4 v[18:21], v0, s[92:95], s56 offen
	s_cselect_b64 s[56:57], -1, 0
	v_cndmask_b32_e64 v34, v79, v78, s[56:57]
	v_cndmask_b32_e32 v34, v34, v199, vcc
	s_add_i32 s57, s90, 0xfffc0000
	v_readlane_b32 s56, v34, s91
	s_lshl_b32 s56, s56, 10
	s_and_b32 s57, s57, 0x1000000
	s_add_i32 s56, s56, s57
	s_add_i32 s91, s63, -1
	s_bitcmp0_b32 s91, 6
	buffer_load_dwordx4 v[34:37], v0, s[92:95], s56 offen
	s_cselect_b64 s[56:57], -1, 0
	v_cndmask_b32_e64 v50, v79, v78, s[56:57]
	v_cndmask_b32_e32 v50, v50, v199, vcc
	s_add_i32 s57, s90, 0xfffe0000
	v_readlane_b32 s56, v50, s91
	s_lshl_b32 s56, s56, 10
	s_and_b32 s57, s57, 0x1000000
	s_add_i32 s56, s56, s57
	s_bitcmp0_b32 s63, 6
	s_nop 0
	buffer_load_dwordx4 v[50:53], v0, s[92:95], s56 offen
	s_cselect_b64 s[56:57], -1, 0
	v_cndmask_b32_e64 v62, v79, v78, s[56:57]
	v_cndmask_b32_e32 v62, v62, v199, vcc
	s_and_b32 s57, s90, 0x1000000
	v_readlane_b32 s56, v62, s63
	s_lshl_b32 s56, s56, 10
	s_add_i32 s56, s56, s57
	s_nop 2
	buffer_load_dwordx4 v[62:65], v0, s[92:95], s56 offen
	s_add_i32 s62, s62, 1
	s_add_i32 s63, s63, 16
	s_add_i32 s90, s90, 0x200000
	s_cmpk_eq_i32 s63, 0x11f
	s_cbranch_scc0 .LBB0_1425
; __device__ __forceinline__ int ov(int x) { asm volatile("" : "+v"(x)); return x; }
;     ...
;         f32x2 acc[16];
;         { const float fsc = wm * (1.0f / 127.0f);
; #pragma unroll
;           for (int i = 0; i < 16; ++i) acc[i] = (f32x2){(float)(acci[2 * i] - acci[2 * i + 1] - c8) * fsc, (float)acci[2 * i + 1] * (fsc * 0.0625f)}; }
;         const int lane2 = ov(lane);
;         float s = 0.f;
; #pragma unroll
;         for (int hh = 0; hh < 4; ++hh) { float pl[8]; unpack8(*(const v4u*)(PLE + (size_t)t * D + lane2 * 32 + hh * 8), pl);
;             float z8[8]; unpack8(*(const v4u*)(ZB + (size_t)t * D + lane2 * 32 + hh * 8), z8);
;             f32x4 xa = (f32x4){z8[0], z8[1], z8[2], z8[3]}, xb = (f32x4){z8[4], z8[5], z8[6], z8[7]};
;             xa = (xa - mean1) * rstd1 * *(const f32x4*)(gain1 + lane2 * 32 + hh * 8) + *(const f32x4*)(bias1 + lane2 * 32 + hh * 8);
;             xb = (xb - mean1) * rstd1 * *(const f32x4*)(gain1 + lane2 * 32 + hh * 8 + 4) + *(const f32x4*)(bias1 + lane2 * 32 + hh * 8 + 4);
	s_waitcnt lgkmcnt(0)
	v_add_f32_e32 v78, v103, v104
	v_cvt_i32_f32_e32 v78, v78
	v_mov_b32_e32 v201, v130
	s_lshl_b64 s[56:57], s[86:87], 1
	v_lshlrev_b32_e32 v78, 3, v78
	v_sub_u32_e32 v78, 0, v78
	v_sub_u32_e32 v79, v78, v69
	v_add_u32_e32 v66, v79, v66
	v_sub_u32_e32 v79, v78, v70
	v_add_u32_e32 v74, v79, v74
	v_sub_u32_e32 v79, v78, v72
	v_add_u32_e32 v75, v79, v75
	v_sub_u32_e32 v79, v78, v73
	v_add_u32_e32 v76, v79, v76
	v_sub_u32_e32 v79, v78, v77
	v_add_u32_e32 v79, v79, v80
	v_sub_u32_e32 v80, v78, v81
	v_add_u32_e32 v80, v80, v85
	v_sub_u32_e32 v85, v78, v82
	v_add_u32_e32 v85, v85, v86
	v_sub_u32_e32 v86, v78, v84
	v_add_u32_e32 v86, v86, v94
	v_sub_u32_e32 v94, v78, v87
	v_add_u32_e32 v94, v94, v95
	v_sub_u32_e32 v95, v78, v88
	v_readlane_b32 s62, v255, 7
	v_lshlrev_b32_e32 v134, 5, v201
	v_add_u32_e32 v95, v95, v96
	v_sub_u32_e32 v96, v78, v89
	s_add_u32 s62, s62, s56
	v_readlane_b32 s63, v255, 9
	v_ashrrev_i32_e32 v135, 31, v134
	v_add_u32_e32 v96, v96, v97
	v_sub_u32_e32 v97, v78, v90
	v_cvt_f32_i32_e32 v181, v70
	v_mul_f32_e32 v142, 0x3c010204, v71
	s_addc_u32 s63, s63, s57
	v_lshlrev_b64 v[70:71], 1, v[134:135]
	v_add_u32_e32 v97, v97, v98
	v_sub_u32_e32 v98, v78, v91
	v_cvt_f32_i32_e32 v178, v75
	v_cvt_f32_i32_e32 v180, v74
	v_lshl_add_u64 v[74:75], s[62:63], 0, v[70:71]
	v_readlane_b32 s62, v254, 56
	v_add_u32_e32 v98, v98, v99
	v_sub_u32_e32 v99, v78, v92
	s_add_u32 s62, s62, s56
	v_readlane_b32 s63, v255, 5
	v_add_u32_e32 v99, v99, v100
	v_sub_u32_e32 v100, v78, v93
	v_sub_u32_e32 v78, v78, v83
	s_addc_u32 s63, s63, s57
	v_add_u32_e32 v100, v100, v101
	v_add_u32_e32 v78, v78, v102
	v_cvt_f32_i32_e32 v138, v99
	v_cvt_f32_i32_e32 v140, v98
	v_lshl_add_u64 v[98:99], s[62:63], 0, v[70:71]
	v_cvt_f32_i32_e32 v136, v100
	v_cvt_f32_i32_e32 v137, v93
	v_cvt_f32_i32_e32 v139, v92
	v_cvt_f32_i32_e32 v141, v91
	v_cvt_f32_i32_e32 v146, v97
	v_cvt_f32_i32_e32 v147, v90
	v_cvt_f32_i32_e32 v148, v96
	v_cvt_f32_i32_e32 v149, v89
	v_cvt_f32_i32_e32 v150, v95
	v_cvt_f32_i32_e32 v151, v88
	v_cvt_f32_i32_e32 v152, v94
	v_cvt_f32_i32_e32 v153, v87
	v_cvt_f32_i32_e32 v160, v86
	v_cvt_f32_i32_e32 v161, v84
	v_cvt_f32_i32_e32 v170, v85
	v_cvt_f32_i32_e32 v171, v82
	v_cvt_f32_i32_e32 v172, v80
	v_cvt_f32_i32_e32 v173, v81
	v_cvt_f32_i32_e32 v174, v79
	v_cvt_f32_i32_e32 v175, v77
	v_cvt_f32_i32_e32 v176, v76
	v_cvt_f32_i32_e32 v177, v73
	v_cvt_f32_i32_e32 v179, v72
	v_cvt_f32_i32_e32 v144, v78
	v_cvt_f32_i32_e32 v145, v83
	v_mov_b32_e32 v70, v212
	v_mov_b32_e32 v71, v213
	v_mov_b32_e32 v72, v214
	v_mov_b32_e32 v73, v215
	v_mov_b32_e32 v78, v216
	v_mov_b32_e32 v79, v217
	v_mov_b32_e32 v80, v218
	v_mov_b32_e32 v81, v219
	v_mov_b32_e32 v86, v220
	v_mov_b32_e32 v87, v221
	v_mov_b32_e32 v88, v222
	v_mov_b32_e32 v89, v223
	v_mov_b32_e32 v90, v224
	v_mov_b32_e32 v91, v225
	v_mov_b32_e32 v92, v226
	v_mov_b32_e32 v93, v227
	v_mov_b32_e32 v74, v228
	v_mov_b32_e32 v75, v229
	v_mov_b32_e32 v76, v230
	v_mov_b32_e32 v77, v231
	v_mov_b32_e32 v82, v232
	v_mov_b32_e32 v83, v233
	v_mov_b32_e32 v84, v234
	v_mov_b32_e32 v85, v235
	v_mov_b32_e32 v94, v236
	v_mov_b32_e32 v95, v237
	v_mov_b32_e32 v96, v238
	v_mov_b32_e32 v97, v239
	v_mov_b32_e32 v98, v240
	v_mov_b32_e32 v99, v241
	v_mov_b32_e32 v100, v242
	v_mov_b32_e32 v101, v243
	v_cvt_f32_i32_e32 v182, v66
	v_cvt_f32_i32_e32 v183, v69
	v_lshlrev_b64 v[154:155], 2, v[134:135]
	v_readlane_b32 s62, v255, 13
	v_lshl_add_u64 v[158:159], s[36:37], 0, v[154:155]
	v_readlane_b32 s63, v255, 14
	v_mul_f32_e32 v143, 0x3d800000, v142
	v_readlane_b32 s72, v254, 20
	v_lshl_add_u64 v[156:157], s[62:63], 0, v[154:155]
	v_readlane_b32 s73, v254, 21
	v_readlane_b32 s72, v255, 15
	v_readlane_b32 s73, v255, 16
	s_lshl_b64 s[62:63], s[86:87], 2
	v_readlane_b32 s74, v254, 22
	v_readlane_b32 s75, v254, 23
	s_add_u32 s62, s74, s62
	s_addc_u32 s63, s75, s63
	s_and_b64 vcc, exec, s[82:83]
	v_readlane_b32 s76, v254, 24
	v_readlane_b32 s77, v254, 25
	v_readlane_b32 s78, v254, 26
	v_readlane_b32 s79, v254, 27
	s_waitcnt vmcnt(0)
	v_readlane_b32 s98, v254, 58
	v_readlane_b32 s99, v255, 1
	s_cmp_lt_i32 s98, 0x4000
	s_cselect_b32 s100, s98, s88
	s_add_i32 s99, s98, s99
	s_cmp_lt_i32 s99, 0x4000
	s_cselect_b32 s99, s99, s100
	s_lshl_b32 s100, s100, 12
	s_lshl_b32 s99, s99, 9
	v_lshl_add_u32 v244, v130, 6, s100
	v_lshl_add_u32 v249, v130, 2, s99
	v_readlane_b32 s100, v255, 7
	v_readlane_b32 s101, v255, 9
	s_nop 4
	global_load_dwordx4 v[212:215], v244, s[100:101] offset:48
	global_load_dwordx4 v[216:219], v244, s[100:101] offset:32
	global_load_dwordx4 v[220:223], v244, s[100:101] offset:16
	global_load_dwordx4 v[224:227], v244, s[100:101]
	v_readlane_b32 s100, v254, 56
	v_readlane_b32 s101, v255, 5
	s_nop 4
	global_load_dwordx4 v[228:231], v244, s[100:101] offset:48
	global_load_dwordx4 v[232:235], v244, s[100:101] offset:32
	global_load_dwordx4 v[236:239], v244, s[100:101] offset:16
	global_load_dwordx4 v[240:243], v244, s[100:101]
	global_load_dword v245, v249, s[70:71] offset:256
	global_load_dword v246, v249, s[40:41] offset:256
	global_load_dword v247, v249, s[40:41]
	global_load_dword v248, v249, s[70:71]
	v_lshlrev_b32_e32 v66, 16, v98
	v_and_b32_e32 v69, 0xffff0000, v98
	v_lshlrev_b32_e32 v98, 16, v99
	v_and_b32_e32 v99, 0xffff0000, v99
	v_lshlrev_b32_e32 v164, 16, v100
	v_and_b32_e32 v165, 0xffff0000, v100
	v_lshlrev_b32_e32 v166, 16, v101
	v_and_b32_e32 v167, 0xffff0000, v101
	v_sub_f32_e32 v99, v99, v67
	v_sub_f32_e32 v98, v98, v67
	v_sub_f32_e32 v101, v69, v67
	v_sub_f32_e32 v100, v66, v67
	v_pk_mul_f32 v[184:185], v[68:69], v[100:101] op_sel_hi:[0,1]
	v_pk_mul_f32 v[186:187], v[68:69], v[98:99] op_sel_hi:[0,1]
	ds_read_b128 v[98:101], v154 offset:48
	ds_read_b128 v[102:105], v154 offset:32
	ds_read_b128 v[106:109], v154 offset:16
	ds_read_b128 v[122:125], v154 offset:0
	ds_read_b128 v[110:113], v154 offset:8240
	ds_read_b128 v[114:117], v154 offset:8224
	ds_read_b128 v[118:121], v154 offset:8208
	ds_read_b128 v[126:129], v154 offset:8192
	s_waitcnt lgkmcnt(0)
;     ...
;         for (int hh = 0; hh < 4; ++hh) { float pl[8]; unpack8(*(const v4u*)(PLE + (size_t)t * D + lane2 * 32 + hh * 8), pl);
;             float z8[8]; unpack8(*(const v4u*)(ZB + (size_t)t * D + lane2 * 32 + hh * 8), z8);
;             f32x4 xa = (f32x4){z8[0], z8[1], z8[2], z8[3]}, xb = (f32x4){z8[4], z8[5], z8[6], z8[7]};
;             xa = (xa - mean1) * rstd1 * *(const f32x4*)(gain1 + lane2 * 32 + hh * 8) + *(const f32x4*)(bias1 + lane2 * 32 + hh * 8);
;             xb = (xb - mean1) * rstd1 * *(const f32x4*)(gain1 + lane2 * 32 + hh * 8 + 4) + *(const f32x4*)(bias1 + lane2 * 32 + hh * 8 + 4);
;             acc[hh * 4 + 0] += (f32x2){ALPHA * xa[0] + pl[0], ALPHA * xa[1] + pl[1]}; acc[hh * 4 + 1] += (f32x2){ALPHA * xa[2] + pl[2], ALPHA * xa[3] + pl[3]};
;             acc[hh * 4 + 2] += (f32x2){ALPHA * xb[0] + pl[4], ALPHA * xb[1] + pl[5]}; acc[hh * 4 + 3] += (f32x2){ALPHA * xb[2] + pl[6], ALPHA * xb[3] + pl[7]};
; #pragma unroll
;             for (int i = 0; i < 4; ++i) s += acc[hh * 4 + i].x + acc[hh * 4 + i].y; }
	v_pk_fma_f32 v[124:125], v[124:125], v[186:187], v[128:129]
	v_sub_f32_e32 v129, v165, v67
	v_sub_f32_e32 v128, v164, v67
	v_pk_mul_f32 v[128:129], v[68:69], v[128:129] op_sel_hi:[0,1]
	v_pk_fma_f32 v[122:123], v[122:123], v[184:185], v[126:127]
	v_sub_f32_e32 v127, v167, v67
	v_sub_f32_e32 v126, v166, v67
	v_pk_fma_f32 v[106:107], v[106:107], v[128:129], v[118:119]
	v_lshlrev_b32_e32 v118, 16, v90
	v_and_b32_e32 v119, 0xffff0000, v90
	v_lshlrev_b32_e32 v90, 16, v91
	v_and_b32_e32 v91, 0xffff0000, v91
	v_pk_mul_f32 v[126:127], v[68:69], v[126:127] op_sel_hi:[0,1]
	v_pk_fma_f32 v[90:91], v[124:125], s[58:59], v[90:91] op_sel_hi:[1,0,1]
	v_pk_fma_f32 v[108:109], v[108:109], v[126:127], v[120:121]
	v_pk_fma_f32 v[118:119], v[122:123], s[58:59], v[118:119] op_sel_hi:[1,0,1]
	v_pk_fma_f32 v[120:121], v[142:143], v[180:181], v[90:91]
	v_lshlrev_b32_e32 v90, 16, v92
	v_and_b32_e32 v91, 0xffff0000, v92
	v_pk_fma_f32 v[118:119], v[142:143], v[182:183], v[118:119]
	v_pk_fma_f32 v[90:91], v[106:107], s[58:59], v[90:91] op_sel_hi:[1,0,1]
	v_add_f32_e32 v66, v118, v119
	v_pk_fma_f32 v[122:123], v[142:143], v[178:179], v[90:91]
	v_lshlrev_b32_e32 v90, 16, v93
	v_and_b32_e32 v91, 0xffff0000, v93
	v_pk_fma_f32 v[90:91], v[108:109], s[58:59], v[90:91] op_sel_hi:[1,0,1]
	v_add_f32_e32 v66, 0, v66
	v_add_f32_e32 v69, v120, v121
	v_pk_fma_f32 v[124:125], v[142:143], v[176:177], v[90:91]
	v_add_f32_e32 v66, v69, v66
	v_add_f32_e32 v69, v122, v123
	v_add_f32_e32 v66, v69, v66
	v_add_f32_e32 v69, v124, v125
	v_lshlrev_b32_e32 v90, 16, v95
	v_and_b32_e32 v91, 0xffff0000, v95
	v_lshlrev_b32_e32 v106, 16, v96
	v_and_b32_e32 v96, 0xffff0000, v96
	v_add_f32_e32 v66, v69, v66
	v_lshlrev_b32_e32 v69, 16, v94
	v_and_b32_e32 v92, 0xffff0000, v94
	v_lshlrev_b32_e32 v94, 16, v97
	v_and_b32_e32 v95, 0xffff0000, v97
	v_sub_f32_e32 v91, v91, v67
	v_sub_f32_e32 v90, v90, v67
	v_sub_f32_e32 v97, v96, v67
	v_sub_f32_e32 v96, v106, v67
	v_sub_f32_e32 v93, v92, v67
	v_sub_f32_e32 v92, v69, v67
	v_pk_mul_f32 v[90:91], v[68:69], v[90:91] op_sel_hi:[0,1]
	v_pk_mul_f32 v[96:97], v[68:69], v[96:97] op_sel_hi:[0,1]
	v_pk_mul_f32 v[92:93], v[68:69], v[92:93] op_sel_hi:[0,1]
	v_pk_fma_f32 v[90:91], v[104:105], v[90:91], v[116:117]
	v_pk_fma_f32 v[96:97], v[98:99], v[96:97], v[110:111]
	v_lshlrev_b32_e32 v98, 16, v86
	v_and_b32_e32 v99, 0xffff0000, v86
	v_lshlrev_b32_e32 v86, 16, v87
	v_and_b32_e32 v87, 0xffff0000, v87
	v_pk_fma_f32 v[92:93], v[102:103], v[92:93], v[114:115]
	v_pk_fma_f32 v[86:87], v[90:91], s[58:59], v[86:87] op_sel_hi:[1,0,1]
	v_sub_f32_e32 v95, v95, v67
	v_sub_f32_e32 v94, v94, v67
	v_pk_fma_f32 v[92:93], v[92:93], s[58:59], v[98:99] op_sel_hi:[1,0,1]
	v_pk_fma_f32 v[116:117], v[142:143], v[172:173], v[86:87]
	v_lshlrev_b32_e32 v86, 16, v88
	v_and_b32_e32 v87, 0xffff0000, v88
	v_pk_mul_f32 v[94:95], v[68:69], v[94:95] op_sel_hi:[0,1]
	v_pk_fma_f32 v[114:115], v[142:143], v[174:175], v[92:93]
	v_pk_fma_f32 v[86:87], v[96:97], s[58:59], v[86:87] op_sel_hi:[1,0,1]
	v_pk_fma_f32 v[94:95], v[100:101], v[94:95], v[112:113]
	v_pk_fma_f32 v[126:127], v[142:143], v[170:171], v[86:87]
	v_lshlrev_b32_e32 v86, 16, v89
	v_and_b32_e32 v87, 0xffff0000, v89
	v_add_f32_e32 v69, v114, v115
	v_pk_fma_f32 v[86:87], v[94:95], s[58:59], v[86:87] op_sel_hi:[1,0,1]
	v_add_f32_e32 v66, v66, v69
	v_add_f32_e32 v69, v116, v117
	v_pk_fma_f32 v[128:129], v[142:143], v[160:161], v[86:87]
	v_add_f32_e32 v66, v69, v66
	v_add_f32_e32 v69, v126, v127
	v_add_f32_e32 v66, v69, v66
	v_add_f32_e32 v69, v128, v129
	v_lshlrev_b32_e32 v86, 16, v82
	v_and_b32_e32 v87, 0xffff0000, v82
	v_lshlrev_b32_e32 v82, 16, v83
	v_and_b32_e32 v83, 0xffff0000, v83
	v_add_f32_e32 v66, v69, v66
	v_lshlrev_b32_e32 v69, 16, v84
	v_and_b32_e32 v172, 0xffff0000, v84
	v_lshlrev_b32_e32 v173, 16, v85
	v_and_b32_e32 v174, 0xffff0000, v85
	v_sub_f32_e32 v83, v83, v67
	v_sub_f32_e32 v82, v82, v67
	v_sub_f32_e32 v85, v87, v67
	v_sub_f32_e32 v84, v86, v67
	v_pk_mul_f32 v[160:161], v[68:69], v[84:85] op_sel_hi:[0,1]
	v_pk_mul_f32 v[170:171], v[68:69], v[82:83] op_sel_hi:[0,1]
	ds_read_b128 v[82:85], v154 offset:112
	ds_read_b128 v[86:89], v154 offset:96
	ds_read_b128 v[90:93], v154 offset:80
	ds_read_b128 v[106:109], v154 offset:64
	ds_read_b128 v[94:97], v154 offset:8304
	ds_read_b128 v[98:101], v154 offset:8288
	ds_read_b128 v[102:105], v154 offset:8272
	ds_read_b128 v[110:113], v154 offset:8256
	s_waitcnt lgkmcnt(0)
; __device__ __forceinline__ int fresh_lane() { unsigned z = 0u; asm volatile("" : "+v"(z)); return (int)__builtin_amdgcn_mbcnt_hi(~0u, __builtin_amdgcn_mbcnt_lo(~0u, z)); }
; __device__ __forceinline__ float shx(float v, int m, int lane) { return __builtin_bit_cast(float, shx_i(__builtin_bit_cast(int, v), m, lane)); }
; __device__ __forceinline__ float wave_sum(float v) {
;     const int l_ = fresh_lane();
; #pragma unroll
;     for (int o = 32; o >= 1; o >>= 1) v += shx(v, o, l_);
;     return v;
;     ...
;         for (int hh = 0; hh < 4; ++hh) { float pl[8]; unpack8(*(const v4u*)(PLE + (size_t)t * D + lane2 * 32 + hh * 8), pl);
;             float z8[8]; unpack8(*(const v4u*)(ZB + (size_t)t * D + lane2 * 32 + hh * 8), z8);
;             f32x4 xa = (f32x4){z8[0], z8[1], z8[2], z8[3]}, xb = (f32x4){z8[4], z8[5], z8[6], z8[7]};
;             xa = (xa - mean1) * rstd1 * *(const f32x4*)(gain1 + lane2 * 32 + hh * 8) + *(const f32x4*)(bias1 + lane2 * 32 + hh * 8);
;             xb = (xb - mean1) * rstd1 * *(const f32x4*)(gain1 + lane2 * 32 + hh * 8 + 4) + *(const f32x4*)(bias1 + lane2 * 32 + hh * 8 + 4);
;             acc[hh * 4 + 0] += (f32x2){ALPHA * xa[0] + pl[0], ALPHA * xa[1] + pl[1]}; acc[hh * 4 + 1] += (f32x2){ALPHA * xa[2] + pl[2], ALPHA * xa[3] + pl[3]};
;             acc[hh * 4 + 2] += (f32x2){ALPHA * xb[0] + pl[4], ALPHA * xb[1] + pl[5]}; acc[hh * 4 + 3] += (f32x2){ALPHA * xb[2] + pl[6], ALPHA * xb[3] + pl[7]};
; #pragma unroll
;             for (int i = 0; i < 4; ++i) s += acc[hh * 4 + i].x + acc[hh * 4 + i].y; }
;         const float mean = wave_sum(s) * (1.0f / D); float q = 0.f;
	v_pk_fma_f32 v[108:109], v[108:109], v[170:171], v[112:113]
	v_sub_f32_e32 v113, v172, v67
	v_sub_f32_e32 v112, v69, v67
	v_pk_mul_f32 v[112:113], v[68:69], v[112:113] op_sel_hi:[0,1]
	v_pk_fma_f32 v[106:107], v[106:107], v[160:161], v[110:111]
	v_sub_f32_e32 v111, v174, v67
	v_sub_f32_e32 v110, v173, v67
	v_pk_fma_f32 v[90:91], v[90:91], v[112:113], v[102:103]
	v_lshlrev_b32_e32 v102, 16, v78
	v_and_b32_e32 v103, 0xffff0000, v78
	v_lshlrev_b32_e32 v78, 16, v79
	v_and_b32_e32 v79, 0xffff0000, v79
	v_pk_mul_f32 v[110:111], v[68:69], v[110:111] op_sel_hi:[0,1]
	v_pk_fma_f32 v[78:79], v[108:109], s[58:59], v[78:79] op_sel_hi:[1,0,1]
	v_pk_fma_f32 v[92:93], v[92:93], v[110:111], v[104:105]
	v_pk_fma_f32 v[102:103], v[106:107], s[58:59], v[102:103] op_sel_hi:[1,0,1]
	v_pk_fma_f32 v[104:105], v[142:143], v[150:151], v[78:79]
	v_lshlrev_b32_e32 v78, 16, v80
	v_and_b32_e32 v79, 0xffff0000, v80
	v_pk_fma_f32 v[102:103], v[142:143], v[152:153], v[102:103]
	v_pk_fma_f32 v[78:79], v[90:91], s[58:59], v[78:79] op_sel_hi:[1,0,1]
	v_add_f32_e32 v69, v102, v103
	v_pk_fma_f32 v[90:91], v[142:143], v[148:149], v[78:79]
	v_lshlrev_b32_e32 v78, 16, v81
	v_and_b32_e32 v79, 0xffff0000, v81
	v_pk_fma_f32 v[78:79], v[92:93], s[58:59], v[78:79] op_sel_hi:[1,0,1]
	v_add_f32_e32 v66, v66, v69
	v_add_f32_e32 v69, v104, v105
	v_pk_fma_f32 v[92:93], v[142:143], v[146:147], v[78:79]
	v_add_f32_e32 v66, v69, v66
	v_add_f32_e32 v69, v90, v91
	v_add_f32_e32 v66, v69, v66
	v_add_f32_e32 v69, v92, v93
	v_add_f32_e32 v106, v69, v66
	v_lshlrev_b32_e32 v66, 16, v74
	v_and_b32_e32 v69, 0xffff0000, v74
	v_lshlrev_b32_e32 v74, 16, v75
	v_and_b32_e32 v75, 0xffff0000, v75
	v_lshlrev_b32_e32 v80, 16, v76
	v_and_b32_e32 v81, 0xffff0000, v76
	v_lshlrev_b32_e32 v78, 16, v77
	v_and_b32_e32 v79, 0xffff0000, v77
	v_sub_f32_e32 v75, v75, v67
	v_sub_f32_e32 v74, v74, v67
	v_sub_f32_e32 v77, v69, v67
	v_sub_f32_e32 v76, v66, v67
	v_pk_mul_f32 v[74:75], v[68:69], v[74:75] op_sel_hi:[0,1]
	v_sub_f32_e32 v79, v79, v67
	v_sub_f32_e32 v78, v78, v67
	v_sub_f32_e32 v81, v81, v67
	v_sub_f32_e32 v80, v80, v67
	v_pk_mul_f32 v[76:77], v[68:69], v[76:77] op_sel_hi:[0,1]
	v_pk_fma_f32 v[74:75], v[88:89], v[74:75], v[100:101]
	v_pk_mul_f32 v[66:67], v[68:69], v[80:81] op_sel_hi:[0,1]
	v_pk_mul_f32 v[68:69], v[68:69], v[78:79] op_sel_hi:[0,1]
	v_lshlrev_b32_e32 v78, 16, v70
	v_and_b32_e32 v79, 0xffff0000, v70
	v_lshlrev_b32_e32 v70, 16, v71
	v_and_b32_e32 v71, 0xffff0000, v71
	v_pk_fma_f32 v[76:77], v[86:87], v[76:77], v[98:99]
	v_pk_fma_f32 v[70:71], v[74:75], s[58:59], v[70:71] op_sel_hi:[1,0,1]
	v_pk_fma_f32 v[68:69], v[84:85], v[68:69], v[96:97]
	v_pk_fma_f32 v[66:67], v[82:83], v[66:67], v[94:95]
	v_pk_fma_f32 v[76:77], v[76:77], s[58:59], v[78:79] op_sel_hi:[1,0,1]
	v_pk_fma_f32 v[96:97], v[142:143], v[138:139], v[70:71]
	v_lshlrev_b32_e32 v70, 16, v72
	v_and_b32_e32 v71, 0xffff0000, v72
	v_pk_fma_f32 v[94:95], v[142:143], v[140:141], v[76:77]
	v_pk_fma_f32 v[66:67], v[66:67], s[58:59], v[70:71] op_sel_hi:[1,0,1]
	v_lshlrev_b32_e32 v70, 16, v73
	v_and_b32_e32 v71, 0xffff0000, v73
	v_pk_fma_f32 v[68:69], v[68:69], s[58:59], v[70:71] op_sel_hi:[1,0,1]
	v_mov_b32_e32 v70, v96
	v_mov_b32_e32 v71, v94
	v_mov_b32_e32 v72, v97
	v_mov_b32_e32 v73, v95
	v_pk_add_f32 v[70:71], v[70:71], v[72:73]
	v_pk_fma_f32 v[66:67], v[142:143], v[136:137], v[66:67]
	v_pk_fma_f32 v[68:69], v[142:143], v[144:145], v[68:69]
	v_add_f32_e32 v71, v106, v71
	v_add_f32_e32 v74, v70, v71
	v_mov_b32_e32 v70, v68
	v_mov_b32_e32 v71, v66
	v_mov_b32_e32 v72, v69
	v_mov_b32_e32 v73, v67
	v_pk_add_f32 v[70:71], v[70:71], v[72:73]
	v_lshl_add_u64 v[100:101], s[72:73], 0, v[154:155]
	v_add_f32_e32 v71, v71, v74
	v_add_f32_e32 v70, v70, v71
	v_mov_b32_e32 v71, v1
	v_lshl_add_u64 v[98:99], s[62:63], 0, v[154:155]
	v_mbcnt_lo_u32_b32 v71, -1, v71
	v_mbcnt_hi_u32_b32 v71, -1, v71
	v_lshlrev_b32_e32 v71, 2, v71
	v_xor_b32_e32 v72, 0x80, v71
	ds_bpermute_b32 v72, v72, v70
	s_waitcnt lgkmcnt(0)
	v_add_f32_e32 v70, v70, v72
	v_xor_b32_e32 v72, 64, v71
	ds_bpermute_b32 v72, v72, v70
	s_waitcnt lgkmcnt(0)
	v_add_f32_e32 v70, v70, v72
	v_xor_b32_e32 v72, 32, v71
	ds_bpermute_b32 v72, v72, v70
	s_waitcnt lgkmcnt(0)
	v_add_f32_e32 v70, v70, v72
	v_xor_b32_e32 v72, 16, v71
	ds_bpermute_b32 v72, v72, v70
	s_waitcnt lgkmcnt(0)
	v_add_f32_e32 v70, v70, v72
	v_xor_b32_e32 v72, 8, v71
	ds_bpermute_b32 v72, v72, v70
	v_xor_b32_e32 v71, 4, v71
	s_waitcnt lgkmcnt(0)
	v_add_f32_e32 v70, v70, v72
	ds_bpermute_b32 v71, v71, v70
	s_waitcnt lgkmcnt(0)
; __device__ __forceinline__ float ln_rstd(float q) { return __builtin_amdgcn_rsqf((q + LN_EPS * (float)D) * (1.0f / D)); }
; __device__ __forceinline__ v4u pack8(const float (&v)[8]) { v4u o; o.x = pk2(v[0], v[1]); o.y = pk2(v[2], v[3]); o.z = pk2(v[4], v[5]); o.w = pk2(v[6], v[7]); return o; }
;     ...
;         const float mean = wave_sum(s) * (1.0f / D); float q = 0.f;
; #pragma unroll
;         for (int i = 0; i < 16; ++i) { acc[i].x -= mean; acc[i].y -= mean; q += acc[i].x * acc[i].x + acc[i].y * acc[i].y; }
;         const float rstd = ln_rstd(wave_sum(q));
; #pragma unroll
;         for (int hh = 0; hh < 4; ++hh) {
;             const int c = lane2 * 32 + hh * 8;
;             float y[8];
; #pragma unroll
;             for (int q4 = 0; q4 < 2; ++q4) { const f32x4 ga = *(const f32x4*)(gain + c + q4 * 4), ba = *(const f32x4*)(bias + c + q4 * 4);
;                 const f32x2 z0 = acc[hh * 4 + q4 * 2], z1 = acc[hh * 4 + q4 * 2 + 1];
;                 f32x4 yo; yo[0] = z0.x * rstd * ga[0] + ba[0]; yo[1] = z0.y * rstd * ga[1] + ba[1]; yo[2] = z1.x * rstd * ga[2] + ba[2]; yo[3] = z1.y * rstd * ga[3] + ba[3];
;                 if (OF) *(f32x4*)(OF + (size_t)t * D + c + q4 * 4) = yo;
;                 y[q4 * 4] = yo[0]; y[q4 * 4 + 1] = yo[1]; y[q4 * 4 + 2] = yo[2]; y[q4 * 4 + 3] = yo[3]; }
;             if (!OF) *(v4u*)(XB + (size_t)t * D + c) = pack8(y);
	v_add_f32_e32 v70, v70, v71
	v_mul_f32_e32 v110, 0x3a000000, v70
	v_pk_add_f32 v[86:87], v[90:91], v[110:111] op_sel_hi:[1,0] neg_lo:[0,1] neg_hi:[0,1]
	v_pk_add_f32 v[88:89], v[92:93], v[110:111] op_sel_hi:[1,0] neg_lo:[0,1] neg_hi:[0,1]
	v_pk_add_f32 v[90:91], v[94:95], v[110:111] op_sel_hi:[1,0] neg_lo:[0,1] neg_hi:[0,1]
	v_pk_add_f32 v[92:93], v[96:97], v[110:111] op_sel_hi:[1,0] neg_lo:[0,1] neg_hi:[0,1]
	v_pk_add_f32 v[96:97], v[66:67], v[110:111] op_sel_hi:[1,0] neg_lo:[0,1] neg_hi:[0,1]
	v_pk_add_f32 v[94:95], v[68:69], v[110:111] op_sel_hi:[1,0] neg_lo:[0,1] neg_hi:[0,1]
	v_mov_b32_e32 v69, v97
	v_mov_b32_e32 v68, v95
	v_mov_b32_e32 v66, v94
	v_mov_b32_e32 v67, v96
	v_pk_mul_f32 v[68:69], v[68:69], v[68:69]
	v_pk_add_f32 v[82:83], v[102:103], v[110:111] op_sel_hi:[1,0] neg_lo:[0,1] neg_hi:[0,1]
	v_pk_fma_f32 v[144:145], v[66:67], v[66:67], v[68:69]
	v_mov_b32_e32 v66, v1
	v_lshl_add_u64 v[102:103], s[80:81], 0, v[154:155]
	v_mbcnt_lo_u32_b32 v66, -1, v66
	v_mbcnt_hi_u32_b32 v66, -1, v66
	v_lshlrev_b32_e32 v66, 2, v66
	v_xor_b32_e32 v148, 0x80, v66
	v_xor_b32_e32 v149, 64, v66
	v_xor_b32_e32 v150, 32, v66
	v_xor_b32_e32 v151, 16, v66
	v_xor_b32_e32 v152, 8, v66
	v_xor_b32_e32 v153, 4, v66
	ds_read_b128 v[66:69], v154 offset:16384
	ds_read_b128 v[106:109], v154 offset:24576
	v_pk_add_f32 v[70:71], v[122:123], v[110:111] op_sel_hi:[1,0] neg_lo:[0,1] neg_hi:[0,1]
	v_pk_add_f32 v[72:73], v[124:125], v[110:111] op_sel_hi:[1,0] neg_lo:[0,1] neg_hi:[0,1]
	v_pk_add_f32 v[74:75], v[114:115], v[110:111] op_sel_hi:[1,0] neg_lo:[0,1] neg_hi:[0,1]
	v_pk_add_f32 v[76:77], v[116:117], v[110:111] op_sel_hi:[1,0] neg_lo:[0,1] neg_hi:[0,1]
	v_pk_add_f32 v[78:79], v[126:127], v[110:111] op_sel_hi:[1,0] neg_lo:[0,1] neg_hi:[0,1]
	v_pk_add_f32 v[80:81], v[128:129], v[110:111] op_sel_hi:[1,0] neg_lo:[0,1] neg_hi:[0,1]
	v_pk_add_f32 v[84:85], v[104:105], v[110:111] op_sel_hi:[1,0] neg_lo:[0,1] neg_hi:[0,1]
	v_pk_add_f32 v[118:119], v[118:119], v[110:111] op_sel_hi:[1,0] neg_lo:[0,1] neg_hi:[0,1]
	v_pk_add_f32 v[110:111], v[120:121], v[110:111] op_sel_hi:[1,0] neg_lo:[0,1] neg_hi:[0,1]
	v_pk_mul_f32 v[146:147], v[118:119], v[118:119]
	v_pk_mul_f32 v[120:121], v[110:111], v[110:111]
	v_pk_mul_f32 v[112:113], v[70:71], v[70:71]
	v_add_f32_e32 v120, v120, v121
	v_add_f32_e32 v121, v146, v147
	v_pk_mul_f32 v[122:123], v[72:73], v[72:73]
	v_add_f32_e32 v120, v121, v120
	v_add_f32_e32 v112, v112, v113
	v_pk_mul_f32 v[114:115], v[74:75], v[74:75]
	v_add_f32_e32 v112, v112, v120
	v_add_f32_e32 v113, v122, v123
	v_pk_mul_f32 v[116:117], v[76:77], v[76:77]
	v_add_f32_e32 v112, v113, v112
	v_add_f32_e32 v113, v114, v115
	v_pk_mul_f32 v[124:125], v[78:79], v[78:79]
	v_add_f32_e32 v112, v113, v112
	v_add_f32_e32 v113, v116, v117
	v_pk_mul_f32 v[126:127], v[80:81], v[80:81]
	v_add_f32_e32 v112, v113, v112
	v_add_f32_e32 v113, v124, v125
	v_pk_mul_f32 v[128:129], v[82:83], v[82:83]
	v_add_f32_e32 v112, v113, v112
	v_add_f32_e32 v113, v126, v127
	v_pk_mul_f32 v[104:105], v[84:85], v[84:85]
	v_add_f32_e32 v112, v113, v112
	v_add_f32_e32 v113, v128, v129
	v_pk_mul_f32 v[136:137], v[86:87], v[86:87]
	v_add_f32_e32 v112, v113, v112
	v_add_f32_e32 v104, v104, v105
	v_pk_mul_f32 v[138:139], v[88:89], v[88:89]
	v_add_f32_e32 v104, v104, v112
	v_add_f32_e32 v105, v136, v137
	v_pk_mul_f32 v[140:141], v[90:91], v[90:91]
	v_add_f32_e32 v104, v105, v104
	v_add_f32_e32 v105, v138, v139
	v_pk_mul_f32 v[142:143], v[92:93], v[92:93]
	v_add_f32_e32 v104, v105, v104
	v_add_f32_e32 v105, v140, v141
	v_add_f32_e32 v104, v105, v104
	v_add_f32_e32 v105, v142, v143
	v_add_f32_e32 v104, v105, v104
	v_add_f32_e32 v104, v145, v104
	v_add_f32_e32 v104, v144, v104
	ds_bpermute_b32 v105, v148, v104
	s_waitcnt lgkmcnt(0)
	v_add_f32_e32 v104, v104, v105
	ds_bpermute_b32 v105, v149, v104
	s_waitcnt lgkmcnt(0)
	v_add_f32_e32 v104, v104, v105
	ds_bpermute_b32 v105, v150, v104
	s_waitcnt lgkmcnt(0)
	v_add_f32_e32 v104, v104, v105
	ds_bpermute_b32 v105, v151, v104
	s_waitcnt lgkmcnt(0)
	v_add_f32_e32 v104, v104, v105
	ds_bpermute_b32 v105, v152, v104
	s_waitcnt lgkmcnt(0)
	v_add_f32_e32 v104, v104, v105
	ds_bpermute_b32 v105, v153, v104
	s_waitcnt lgkmcnt(0)
	v_add_f32_e32 v104, v104, v105
	v_add_f32_e32 v104, 0x3ca7c5ac, v104
	v_mul_f32_e32 v104, 0x3a000000, v104
	v_rsq_f32_e32 v104, v104
	s_nop 0
	v_pk_mul_f32 v[112:113], v[118:119], v[104:105] op_sel_hi:[1,0]
	s_nop 0
	v_pk_fma_f32 v[66:67], v[66:67], v[112:113], v[106:107]
	v_pk_mul_f32 v[106:107], v[110:111], v[104:105] op_sel_hi:[1,0]
	s_nop 0
	v_pk_fma_f32 v[68:69], v[68:69], v[106:107], v[108:109]
	s_cbranch_vccz .LBB0_1428
	global_store_dwordx4 v[98:99], v[66:69], off
